# baseline (speedup 1.0000x reference)
.LBB3_11:
	s_lshl_b32 s58, s42, 7
	s_add_i32 s59, s41, 0x400
	s_lshr_b32 s59, s59, 6
	s_bfe_u32 s60, s20, 0x1000c
	s_add_i32 s59, s59, s60
	s_lshl_b32 s59, s59, 19
	s_add_u32 s58, s58, s59
	s_add_u32 s58, s56, s58
	s_addc_u32 s59, s57, 0
	s_add_u32 s60, s58, 0x4000
	s_addc_u32 s61, s59, 0
	s_add_u32 s62, s58, 0x100000
	s_addc_u32 s63, s59, 0
	s_add_u32 s64, s62, 0x4000
	s_addc_u32 s65, s63, 0
	s_lshr_b32 s66, s41, 7
	s_bfe_u32 s67, s20, 0x1000c
	s_add_i32 s66, s66, s67
	s_lshl_b32 s66, s66, 14
	s_lshl_b32 s67, s42, 2
	s_add_u32 s66, s66, s67
	s_add_u32 s66, s14, s66
	s_addc_u32 s67, s15, 0
	v_add_u32_e32 v172, s43, v207
	v_pk_fma_f32 v[244:245], v[244:245], -0.5, -0.5 op_sel_hi:[1,0,0]
	v_pk_fma_f32 v[246:247], v[246:247], -0.5, -0.5 op_sel_hi:[1,0,0]
	v_pk_fma_f32 v[248:249], v[248:249], -0.5, -0.5 op_sel_hi:[1,0,0]
	v_pk_fma_f32 v[250:251], v[250:251], -0.5, -0.5 op_sel_hi:[1,0,0]
	v_pk_fma_f32 v[252:253], v[252:253], -0.5, -0.5 op_sel_hi:[1,0,0]
	v_pk_fma_f32 v[254:255], v[254:255], -0.5, -0.5 op_sel_hi:[1,0,0]
	v_pk_fma_f32 v[232:233], v[232:233], -0.5, -0.5 op_sel_hi:[1,0,0]
	v_pk_fma_f32 v[234:235], v[234:235], -0.5, -0.5 op_sel_hi:[1,0,0]
	v_pk_mul_f32 v[134:135], v[244:245], v[246:247]
	v_pk_mul_f32 v[146:147], v[248:249], v[250:251]
	v_pk_mul_f32 v[180:181], v[252:253], v[254:255]
	v_pk_mul_f32 v[236:237], v[232:233], v[234:235]
	v_mul_f32_e32 v138, v134, v135
	v_mul_f32_e32 v150, v146, v147
	v_mul_f32_e32 v184, v180, v181
	v_mul_f32_e32 v240, v236, v237
	v_rcp_f32_e32 v138, v138
	v_rcp_f32_e32 v150, v150
	v_rcp_f32_e32 v184, v184
	v_rcp_f32_e32 v240, v240
	v_pk_add_f32 v[164:165], v[114:115], v[116:117]
	v_pk_add_f32 v[164:165], v[164:165], v[78:79]
	v_pk_add_f32 v[164:165], v[164:165], v[80:81]
	v_pk_add_f32 v[164:165], v[164:165], v[106:107]
	v_pk_add_f32 v[164:165], v[164:165], v[108:109]
	v_pk_add_f32 v[164:165], v[164:165], v[70:71]
	v_pk_add_f32 v[164:165], v[164:165], v[72:73]
	v_pk_mul_f32 v[162:163], v[134:135], v[146:147]
	v_pk_mul_f32 v[162:163], v[162:163], v[180:181]
	v_pk_mul_f32 v[162:163], v[162:163], v[236:237]
	v_pk_mul_f32 v[136:137], v[138:139], v[134:135] op_sel:[0,1] op_sel_hi:[0,0]
	v_pk_mul_f32 v[148:149], v[150:151], v[146:147] op_sel:[0,1] op_sel_hi:[0,0]
	v_pk_mul_f32 v[182:183], v[184:185], v[180:181] op_sel:[0,1] op_sel_hi:[0,0]
	v_pk_mul_f32 v[238:239], v[240:241], v[236:237] op_sel:[0,1] op_sel_hi:[0,0]
	v_pk_fma_f32 v[138:139], v[136:137], v[246:247], 1.0 op_sel_hi:[1,1,0]
	v_pk_fma_f32 v[140:141], v[136:137], v[244:245], 1.0 op_sel_hi:[1,1,0]
	v_pk_fma_f32 v[150:151], v[148:149], v[250:251], 1.0 op_sel_hi:[1,1,0]
	v_pk_fma_f32 v[152:153], v[148:149], v[248:249], 1.0 op_sel_hi:[1,1,0]
	v_pk_fma_f32 v[184:185], v[182:183], v[254:255], 1.0 op_sel_hi:[1,1,0]
	v_pk_fma_f32 v[186:187], v[182:183], v[252:253], 1.0 op_sel_hi:[1,1,0]
	v_pk_fma_f32 v[240:241], v[238:239], v[234:235], 1.0 op_sel_hi:[1,1,0]
	v_pk_fma_f32 v[242:243], v[238:239], v[232:233], 1.0 op_sel_hi:[1,1,0]
	v_cvt_pk_bf16_f32 v154, v138, v139
	v_cvt_pk_bf16_f32 v155, v140, v141
	v_cvt_pk_bf16_f32 v156, v150, v151
	v_cvt_pk_bf16_f32 v157, v152, v153
	v_cvt_pk_bf16_f32 v158, v184, v185
	v_cvt_pk_bf16_f32 v159, v186, v187
	v_cvt_pk_bf16_f32 v160, v240, v241
	v_cvt_pk_bf16_f32 v161, v242, v243
	ds_read_b128 v[114:117], v172
	ds_read_b128 v[78:81], v172 offset:64
	ds_read_b128 v[106:109], v172 offset:128
	ds_read_b128 v[70:73], v172 offset:192
	v_permlane16_swap_b32_e32 v154, v156
	v_permlane16_swap_b32_e32 v155, v157
	s_cmp_gt_u32 s40, 4
	s_cbranch_scc1 .Lg1_pl1
	global_store_dwordx4 v228, v[154:157], s[58:59] nt
	s_branch .Lg1_dn1
.Lg1_pl1:
	global_store_dwordx4 v228, v[154:157], s[58:59]
.Lg1_dn1:
	s_bitcmp1_b32 s20, 12
	s_cbranch_scc1 .Lg1_noX
	s_barrier
.Lg1_noX:
	v_permlane16_swap_b32_e32 v158, v160
	v_permlane16_swap_b32_e32 v159, v161
	s_cmp_gt_u32 s40, 4
	s_cbranch_scc1 .Lg1_pl2
	global_store_dwordx4 v228, v[158:161], s[58:59] offset:128 nt
	s_branch .Lg1_dn2
.Lg1_pl2:
	global_store_dwordx4 v228, v[158:161], s[58:59] offset:128
.Lg1_dn2:
	v_exp_f32_e32 v130, v90
	v_exp_f32_e32 v131, v91
	v_exp_f32_e32 v132, v92
	v_exp_f32_e32 v133, v93
	v_exp_f32_e32 v142, v42
	v_exp_f32_e32 v143, v43
	v_exp_f32_e32 v144, v44
	v_exp_f32_e32 v145, v45
	v_exp_f32_e32 v176, v126
	v_exp_f32_e32 v177, v127
	v_exp_f32_e32 v178, v128
	v_exp_f32_e32 v179, v129
	v_exp_f32_e32 v232, v58
	v_exp_f32_e32 v233, v59
	v_exp_f32_e32 v234, v60
	v_exp_f32_e32 v235, v61
	v_pk_fma_f32 v[130:131], v[130:131], -0.5, -0.5 op_sel_hi:[1,0,0]
	v_pk_fma_f32 v[132:133], v[132:133], -0.5, -0.5 op_sel_hi:[1,0,0]
	v_pk_fma_f32 v[142:143], v[142:143], -0.5, -0.5 op_sel_hi:[1,0,0]
	v_pk_fma_f32 v[144:145], v[144:145], -0.5, -0.5 op_sel_hi:[1,0,0]
	v_pk_fma_f32 v[176:177], v[176:177], -0.5, -0.5 op_sel_hi:[1,0,0]
	v_pk_fma_f32 v[178:179], v[178:179], -0.5, -0.5 op_sel_hi:[1,0,0]
	v_pk_fma_f32 v[232:233], v[232:233], -0.5, -0.5 op_sel_hi:[1,0,0]
	v_pk_fma_f32 v[234:235], v[234:235], -0.5, -0.5 op_sel_hi:[1,0,0]
	v_pk_mul_f32 v[134:135], v[130:131], v[132:133]
	v_pk_mul_f32 v[146:147], v[142:143], v[144:145]
	v_pk_mul_f32 v[180:181], v[176:177], v[178:179]
	v_pk_mul_f32 v[236:237], v[232:233], v[234:235]
	v_mul_f32_e32 v138, v134, v135
	v_mul_f32_e32 v150, v146, v147
	v_mul_f32_e32 v184, v180, v181
	v_mul_f32_e32 v240, v236, v237
	v_rcp_f32_e32 v138, v138
	v_rcp_f32_e32 v150, v150
	v_rcp_f32_e32 v184, v184
	v_rcp_f32_e32 v240, v240
	v_pk_add_f32 v[164:165], v[164:165], v[90:91]
	v_pk_add_f32 v[164:165], v[164:165], v[92:93]
	v_pk_add_f32 v[164:165], v[164:165], v[42:43]
	v_pk_add_f32 v[164:165], v[164:165], v[44:45]
	v_pk_add_f32 v[164:165], v[164:165], v[126:127]
	v_pk_add_f32 v[164:165], v[164:165], v[128:129]
	v_pk_add_f32 v[164:165], v[164:165], v[58:59]
	v_pk_add_f32 v[164:165], v[164:165], v[60:61]
	v_pk_mul_f32 v[174:175], v[134:135], v[146:147]
	v_pk_mul_f32 v[174:175], v[174:175], v[180:181]
	v_pk_mul_f32 v[174:175], v[174:175], v[236:237]
	v_pk_mul_f32 v[136:137], v[138:139], v[134:135] op_sel:[0,1] op_sel_hi:[0,0]
	v_pk_mul_f32 v[148:149], v[150:151], v[146:147] op_sel:[0,1] op_sel_hi:[0,0]
	v_pk_mul_f32 v[182:183], v[184:185], v[180:181] op_sel:[0,1] op_sel_hi:[0,0]
	v_pk_mul_f32 v[238:239], v[240:241], v[236:237] op_sel:[0,1] op_sel_hi:[0,0]
	v_pk_fma_f32 v[138:139], v[136:137], v[132:133], 1.0 op_sel_hi:[1,1,0]
	v_pk_fma_f32 v[140:141], v[136:137], v[130:131], 1.0 op_sel_hi:[1,1,0]
	v_pk_fma_f32 v[150:151], v[148:149], v[144:145], 1.0 op_sel_hi:[1,1,0]
	v_pk_fma_f32 v[152:153], v[148:149], v[142:143], 1.0 op_sel_hi:[1,1,0]
	v_pk_fma_f32 v[184:185], v[182:183], v[178:179], 1.0 op_sel_hi:[1,1,0]
	v_pk_fma_f32 v[186:187], v[182:183], v[176:177], 1.0 op_sel_hi:[1,1,0]
	v_pk_fma_f32 v[240:241], v[238:239], v[234:235], 1.0 op_sel_hi:[1,1,0]
	v_pk_fma_f32 v[242:243], v[238:239], v[232:233], 1.0 op_sel_hi:[1,1,0]
	v_cvt_pk_bf16_f32 v154, v138, v139
	v_cvt_pk_bf16_f32 v155, v140, v141
	v_cvt_pk_bf16_f32 v156, v150, v151
	v_cvt_pk_bf16_f32 v157, v152, v153
	v_cvt_pk_bf16_f32 v158, v184, v185
	v_cvt_pk_bf16_f32 v159, v186, v187
	v_cvt_pk_bf16_f32 v160, v240, v241
	v_cvt_pk_bf16_f32 v161, v242, v243
	ds_read_b128 v[90:93], v172 offset:512
	ds_read_b128 v[42:45], v172 offset:576
	ds_read_b128 v[126:129], v172 offset:640
	ds_read_b128 v[58:61], v172 offset:704
	v_permlane16_swap_b32_e32 v154, v156
	v_permlane16_swap_b32_e32 v155, v157
	s_cmp_gt_u32 s40, 4
	s_cbranch_scc1 .Lg1_pl3
	global_store_dwordx4 v228, v[154:157], s[62:63] nt
	s_branch .Lg1_dn3
.Lg1_pl3:
	global_store_dwordx4 v228, v[154:157], s[62:63]
.Lg1_dn3:
	v_permlane16_swap_b32_e32 v158, v160
	v_permlane16_swap_b32_e32 v159, v161
	s_cmp_gt_u32 s40, 4
	s_cbranch_scc1 .Lg1_pl4
	global_store_dwordx4 v228, v[158:161], s[62:63] offset:128 nt
	s_branch .Lg1_dn4
.Lg1_pl4:
	global_store_dwordx4 v228, v[158:161], s[62:63] offset:128
.Lg1_dn4:
	v_log_f32_e32 v166, v162
	v_log_f32_e32 v167, v163
	v_log_f32_e32 v170, v174
	v_log_f32_e32 v171, v175
	v_add_f32_e32 v168, v164, v165
	v_mul_f32_e32 v168, 0xbeb17218, v168
	v_add_f32_e32 v166, v166, v167
	v_add_f32_e32 v170, v170, v171
	v_add_f32_e32 v166, v166, v170
	v_fmac_f32_e32 v168, 0x3f317218, v166
	v_mov_b32_e32 v169, v168
	s_nop 1
	v_permlane16_swap_b32_e32 v168, v169
	v_add_f32_e32 v168, v168, v169
	v_mov_b32_e32 v169, v168
	s_nop 1
	v_permlane32_swap_b32_e32 v168, v169
	v_add_f32_e32 v168, v168, v169
	s_mov_b64 exec, s[0:1]
	global_store_dword v229, v168, s[66:67]
	s_mov_b64 exec, -1
	v_exp_f32_e32 v130, v110
	v_exp_f32_e32 v131, v111
	v_exp_f32_e32 v132, v112
	v_exp_f32_e32 v133, v113
	v_exp_f32_e32 v142, v74
	v_exp_f32_e32 v143, v75
	v_exp_f32_e32 v144, v76
	v_exp_f32_e32 v145, v77
	v_exp_f32_e32 v176, v102
	v_exp_f32_e32 v177, v103
	v_exp_f32_e32 v178, v104
	v_exp_f32_e32 v179, v105
	v_exp_f32_e32 v232, v66
	v_exp_f32_e32 v233, v67
	v_exp_f32_e32 v234, v68
	v_exp_f32_e32 v235, v69
	v_pk_fma_f32 v[130:131], v[130:131], -0.5, -0.5 op_sel_hi:[1,0,0]
	v_pk_fma_f32 v[132:133], v[132:133], -0.5, -0.5 op_sel_hi:[1,0,0]
	v_pk_fma_f32 v[142:143], v[142:143], -0.5, -0.5 op_sel_hi:[1,0,0]
	v_pk_fma_f32 v[144:145], v[144:145], -0.5, -0.5 op_sel_hi:[1,0,0]
	v_pk_fma_f32 v[176:177], v[176:177], -0.5, -0.5 op_sel_hi:[1,0,0]
	v_pk_fma_f32 v[178:179], v[178:179], -0.5, -0.5 op_sel_hi:[1,0,0]
	v_pk_fma_f32 v[232:233], v[232:233], -0.5, -0.5 op_sel_hi:[1,0,0]
	v_pk_fma_f32 v[234:235], v[234:235], -0.5, -0.5 op_sel_hi:[1,0,0]
	v_pk_mul_f32 v[134:135], v[130:131], v[132:133]
	v_pk_mul_f32 v[146:147], v[142:143], v[144:145]
	v_pk_mul_f32 v[180:181], v[176:177], v[178:179]
	v_pk_mul_f32 v[236:237], v[232:233], v[234:235]
	v_mul_f32_e32 v138, v134, v135
	v_mul_f32_e32 v150, v146, v147
	v_mul_f32_e32 v184, v180, v181
	v_mul_f32_e32 v240, v236, v237
	v_rcp_f32_e32 v138, v138
	v_rcp_f32_e32 v150, v150
	v_rcp_f32_e32 v184, v184
	v_rcp_f32_e32 v240, v240
	v_pk_add_f32 v[164:165], v[110:111], v[112:113]
	v_pk_add_f32 v[164:165], v[164:165], v[74:75]
	v_pk_add_f32 v[164:165], v[164:165], v[76:77]
	v_pk_add_f32 v[164:165], v[164:165], v[102:103]
	v_pk_add_f32 v[164:165], v[164:165], v[104:105]
	v_pk_add_f32 v[164:165], v[164:165], v[66:67]
	v_pk_add_f32 v[164:165], v[164:165], v[68:69]
	v_pk_mul_f32 v[162:163], v[134:135], v[146:147]
	v_pk_mul_f32 v[162:163], v[162:163], v[180:181]
	v_pk_mul_f32 v[162:163], v[162:163], v[236:237]
	v_pk_mul_f32 v[136:137], v[138:139], v[134:135] op_sel:[0,1] op_sel_hi:[0,0]
	v_pk_mul_f32 v[148:149], v[150:151], v[146:147] op_sel:[0,1] op_sel_hi:[0,0]
	v_pk_mul_f32 v[182:183], v[184:185], v[180:181] op_sel:[0,1] op_sel_hi:[0,0]
	v_pk_mul_f32 v[238:239], v[240:241], v[236:237] op_sel:[0,1] op_sel_hi:[0,0]
	v_pk_fma_f32 v[138:139], v[136:137], v[132:133], 1.0 op_sel_hi:[1,1,0]
	v_pk_fma_f32 v[140:141], v[136:137], v[130:131], 1.0 op_sel_hi:[1,1,0]
	v_pk_fma_f32 v[150:151], v[148:149], v[144:145], 1.0 op_sel_hi:[1,1,0]
	v_pk_fma_f32 v[152:153], v[148:149], v[142:143], 1.0 op_sel_hi:[1,1,0]
	v_pk_fma_f32 v[184:185], v[182:183], v[178:179], 1.0 op_sel_hi:[1,1,0]
	v_pk_fma_f32 v[186:187], v[182:183], v[176:177], 1.0 op_sel_hi:[1,1,0]
	v_pk_fma_f32 v[240:241], v[238:239], v[234:235], 1.0 op_sel_hi:[1,1,0]
	v_pk_fma_f32 v[242:243], v[238:239], v[232:233], 1.0 op_sel_hi:[1,1,0]
	v_cvt_pk_bf16_f32 v154, v138, v139
	v_cvt_pk_bf16_f32 v155, v140, v141
	v_cvt_pk_bf16_f32 v156, v150, v151
	v_cvt_pk_bf16_f32 v157, v152, v153
	v_cvt_pk_bf16_f32 v158, v184, v185
	v_cvt_pk_bf16_f32 v159, v186, v187
	v_cvt_pk_bf16_f32 v160, v240, v241
	v_cvt_pk_bf16_f32 v161, v242, v243
	ds_read_b128 v[110:113], v172
	ds_read_b128 v[74:77], v172 offset:64
	ds_read_b128 v[102:105], v172 offset:128
	ds_read_b128 v[66:69], v172 offset:192
	v_permlane16_swap_b32_e32 v154, v156
	v_permlane16_swap_b32_e32 v155, v157
	s_cmp_gt_u32 s40, 4
	s_cbranch_scc1 .Lg1_pl5
	global_store_dwordx4 v228, v[154:157], s[58:59] offset:2048 nt
	s_branch .Lg1_dn5
.Lg1_pl5:
	global_store_dwordx4 v228, v[154:157], s[58:59] offset:2048
.Lg1_dn5:
	v_permlane16_swap_b32_e32 v158, v160
	v_permlane16_swap_b32_e32 v159, v161
	s_cmp_gt_u32 s40, 4
	s_cbranch_scc1 .Lg1_pl6
	global_store_dwordx4 v228, v[158:161], s[58:59] offset:2176 nt
	s_branch .Lg1_dn6
.Lg1_pl6:
	global_store_dwordx4 v228, v[158:161], s[58:59] offset:2176
.Lg1_dn6:
	v_exp_f32_e32 v130, v86
	v_exp_f32_e32 v131, v87
	v_exp_f32_e32 v132, v88
	v_exp_f32_e32 v133, v89
	v_exp_f32_e32 v142, v38
	v_exp_f32_e32 v143, v39
	v_exp_f32_e32 v144, v40
	v_exp_f32_e32 v145, v41
	v_exp_f32_e32 v176, v122
	v_exp_f32_e32 v177, v123
	v_exp_f32_e32 v178, v124
	v_exp_f32_e32 v179, v125
	v_exp_f32_e32 v232, v50
	v_exp_f32_e32 v233, v51
	v_exp_f32_e32 v234, v52
	v_exp_f32_e32 v235, v53
	v_pk_fma_f32 v[130:131], v[130:131], -0.5, -0.5 op_sel_hi:[1,0,0]
	v_pk_fma_f32 v[132:133], v[132:133], -0.5, -0.5 op_sel_hi:[1,0,0]
	v_pk_fma_f32 v[142:143], v[142:143], -0.5, -0.5 op_sel_hi:[1,0,0]
	v_pk_fma_f32 v[144:145], v[144:145], -0.5, -0.5 op_sel_hi:[1,0,0]
	v_pk_fma_f32 v[176:177], v[176:177], -0.5, -0.5 op_sel_hi:[1,0,0]
	v_pk_fma_f32 v[178:179], v[178:179], -0.5, -0.5 op_sel_hi:[1,0,0]
	v_pk_fma_f32 v[232:233], v[232:233], -0.5, -0.5 op_sel_hi:[1,0,0]
	v_pk_fma_f32 v[234:235], v[234:235], -0.5, -0.5 op_sel_hi:[1,0,0]
	v_pk_mul_f32 v[134:135], v[130:131], v[132:133]
	v_pk_mul_f32 v[146:147], v[142:143], v[144:145]
	v_pk_mul_f32 v[180:181], v[176:177], v[178:179]
	v_pk_mul_f32 v[236:237], v[232:233], v[234:235]
	v_mul_f32_e32 v138, v134, v135
	v_mul_f32_e32 v150, v146, v147
	v_mul_f32_e32 v184, v180, v181
	v_mul_f32_e32 v240, v236, v237
	v_rcp_f32_e32 v138, v138
	v_rcp_f32_e32 v150, v150
	v_rcp_f32_e32 v184, v184
	v_rcp_f32_e32 v240, v240
	v_pk_add_f32 v[164:165], v[164:165], v[86:87]
	v_pk_add_f32 v[164:165], v[164:165], v[88:89]
	v_pk_add_f32 v[164:165], v[164:165], v[38:39]
	v_pk_add_f32 v[164:165], v[164:165], v[40:41]
	v_pk_add_f32 v[164:165], v[164:165], v[122:123]
	v_pk_add_f32 v[164:165], v[164:165], v[124:125]
	v_pk_add_f32 v[164:165], v[164:165], v[50:51]
	v_pk_add_f32 v[164:165], v[164:165], v[52:53]
	v_pk_mul_f32 v[174:175], v[134:135], v[146:147]
	v_pk_mul_f32 v[174:175], v[174:175], v[180:181]
	v_pk_mul_f32 v[174:175], v[174:175], v[236:237]
	v_pk_mul_f32 v[136:137], v[138:139], v[134:135] op_sel:[0,1] op_sel_hi:[0,0]
	v_pk_mul_f32 v[148:149], v[150:151], v[146:147] op_sel:[0,1] op_sel_hi:[0,0]
	v_pk_mul_f32 v[182:183], v[184:185], v[180:181] op_sel:[0,1] op_sel_hi:[0,0]
	v_pk_mul_f32 v[238:239], v[240:241], v[236:237] op_sel:[0,1] op_sel_hi:[0,0]
	v_pk_fma_f32 v[138:139], v[136:137], v[132:133], 1.0 op_sel_hi:[1,1,0]
	v_pk_fma_f32 v[140:141], v[136:137], v[130:131], 1.0 op_sel_hi:[1,1,0]
	v_pk_fma_f32 v[150:151], v[148:149], v[144:145], 1.0 op_sel_hi:[1,1,0]
	v_pk_fma_f32 v[152:153], v[148:149], v[142:143], 1.0 op_sel_hi:[1,1,0]
	v_pk_fma_f32 v[184:185], v[182:183], v[178:179], 1.0 op_sel_hi:[1,1,0]
	v_pk_fma_f32 v[186:187], v[182:183], v[176:177], 1.0 op_sel_hi:[1,1,0]
	v_pk_fma_f32 v[240:241], v[238:239], v[234:235], 1.0 op_sel_hi:[1,1,0]
	v_pk_fma_f32 v[242:243], v[238:239], v[232:233], 1.0 op_sel_hi:[1,1,0]
	v_cvt_pk_bf16_f32 v154, v138, v139
	v_cvt_pk_bf16_f32 v155, v140, v141
	v_cvt_pk_bf16_f32 v156, v150, v151
	v_cvt_pk_bf16_f32 v157, v152, v153
	v_cvt_pk_bf16_f32 v158, v184, v185
	v_cvt_pk_bf16_f32 v159, v186, v187
	v_cvt_pk_bf16_f32 v160, v240, v241
	v_cvt_pk_bf16_f32 v161, v242, v243
	ds_read_b128 v[86:89], v172 offset:512
	ds_read_b128 v[38:41], v172 offset:576
	ds_read_b128 v[122:125], v172 offset:640
	ds_read_b128 v[50:53], v172 offset:704
	v_permlane16_swap_b32_e32 v154, v156
	v_permlane16_swap_b32_e32 v155, v157
	s_cmp_gt_u32 s40, 4
	s_cbranch_scc1 .Lg1_pl7
	global_store_dwordx4 v228, v[154:157], s[62:63] offset:2048 nt
	s_branch .Lg1_dn7
.Lg1_pl7:
	global_store_dwordx4 v228, v[154:157], s[62:63] offset:2048
.Lg1_dn7:
	v_permlane16_swap_b32_e32 v158, v160
	v_permlane16_swap_b32_e32 v159, v161
	s_cmp_gt_u32 s40, 4
	s_cbranch_scc1 .Lg1_pl8
	global_store_dwordx4 v228, v[158:161], s[62:63] offset:2176 nt
	s_branch .Lg1_dn8
.Lg1_pl8:
	global_store_dwordx4 v228, v[158:161], s[62:63] offset:2176
.Lg1_dn8:
	v_log_f32_e32 v166, v162
	v_log_f32_e32 v167, v163
	v_log_f32_e32 v170, v174
	v_log_f32_e32 v171, v175
	v_add_f32_e32 v168, v164, v165
	v_mul_f32_e32 v168, 0xbeb17218, v168
	v_add_f32_e32 v166, v166, v167
	v_add_f32_e32 v170, v170, v171
	v_add_f32_e32 v166, v166, v170
	v_fmac_f32_e32 v168, 0x3f317218, v166
	v_mov_b32_e32 v169, v168
	s_nop 1
	v_permlane16_swap_b32_e32 v168, v169
	v_add_f32_e32 v168, v168, v169
	v_mov_b32_e32 v169, v168
	s_nop 1
	v_permlane32_swap_b32_e32 v168, v169
	v_add_f32_e32 v168, v168, v169
	s_mov_b64 exec, s[0:1]
	global_store_dword v229, v168, s[66:67] offset:64
	s_mov_b64 exec, -1
	v_exp_f32_e32 v130, v98
	v_exp_f32_e32 v131, v99
	v_exp_f32_e32 v132, v100
	v_exp_f32_e32 v133, v101
	v_exp_f32_e32 v142, v62
	v_exp_f32_e32 v143, v63
	v_exp_f32_e32 v144, v64
	v_exp_f32_e32 v145, v65
	v_exp_f32_e32 v176, v94
	v_exp_f32_e32 v177, v95
	v_exp_f32_e32 v178, v96
	v_exp_f32_e32 v179, v97
	v_exp_f32_e32 v232, v54
	v_exp_f32_e32 v233, v55
	v_exp_f32_e32 v234, v56
	v_exp_f32_e32 v235, v57
	v_pk_fma_f32 v[130:131], v[130:131], -0.5, -0.5 op_sel_hi:[1,0,0]
	v_pk_fma_f32 v[132:133], v[132:133], -0.5, -0.5 op_sel_hi:[1,0,0]
	v_pk_fma_f32 v[142:143], v[142:143], -0.5, -0.5 op_sel_hi:[1,0,0]
	v_pk_fma_f32 v[144:145], v[144:145], -0.5, -0.5 op_sel_hi:[1,0,0]
	v_pk_fma_f32 v[176:177], v[176:177], -0.5, -0.5 op_sel_hi:[1,0,0]
	v_pk_fma_f32 v[178:179], v[178:179], -0.5, -0.5 op_sel_hi:[1,0,0]
	v_pk_fma_f32 v[232:233], v[232:233], -0.5, -0.5 op_sel_hi:[1,0,0]
	v_pk_fma_f32 v[234:235], v[234:235], -0.5, -0.5 op_sel_hi:[1,0,0]
	v_pk_mul_f32 v[134:135], v[130:131], v[132:133]
	v_pk_mul_f32 v[146:147], v[142:143], v[144:145]
	v_pk_mul_f32 v[180:181], v[176:177], v[178:179]
	v_pk_mul_f32 v[236:237], v[232:233], v[234:235]
	v_mul_f32_e32 v138, v134, v135
	v_mul_f32_e32 v150, v146, v147
	v_mul_f32_e32 v184, v180, v181
	v_mul_f32_e32 v240, v236, v237
	v_rcp_f32_e32 v138, v138
	v_rcp_f32_e32 v150, v150
	v_rcp_f32_e32 v184, v184
	v_rcp_f32_e32 v240, v240
	v_pk_add_f32 v[164:165], v[98:99], v[100:101]
	v_pk_add_f32 v[164:165], v[164:165], v[62:63]
	v_pk_add_f32 v[164:165], v[164:165], v[64:65]
	v_pk_add_f32 v[164:165], v[164:165], v[94:95]
	v_pk_add_f32 v[164:165], v[164:165], v[96:97]
	v_pk_add_f32 v[164:165], v[164:165], v[54:55]
	v_pk_add_f32 v[164:165], v[164:165], v[56:57]
	v_pk_mul_f32 v[162:163], v[134:135], v[146:147]
	v_pk_mul_f32 v[162:163], v[162:163], v[180:181]
	v_pk_mul_f32 v[162:163], v[162:163], v[236:237]
	v_pk_mul_f32 v[136:137], v[138:139], v[134:135] op_sel:[0,1] op_sel_hi:[0,0]
	v_pk_mul_f32 v[148:149], v[150:151], v[146:147] op_sel:[0,1] op_sel_hi:[0,0]
	v_pk_mul_f32 v[182:183], v[184:185], v[180:181] op_sel:[0,1] op_sel_hi:[0,0]
	v_pk_mul_f32 v[238:239], v[240:241], v[236:237] op_sel:[0,1] op_sel_hi:[0,0]
	v_pk_fma_f32 v[138:139], v[136:137], v[132:133], 1.0 op_sel_hi:[1,1,0]
	v_pk_fma_f32 v[140:141], v[136:137], v[130:131], 1.0 op_sel_hi:[1,1,0]
	v_pk_fma_f32 v[150:151], v[148:149], v[144:145], 1.0 op_sel_hi:[1,1,0]
	v_pk_fma_f32 v[152:153], v[148:149], v[142:143], 1.0 op_sel_hi:[1,1,0]
	v_pk_fma_f32 v[184:185], v[182:183], v[178:179], 1.0 op_sel_hi:[1,1,0]
	v_pk_fma_f32 v[186:187], v[182:183], v[176:177], 1.0 op_sel_hi:[1,1,0]
	v_pk_fma_f32 v[240:241], v[238:239], v[234:235], 1.0 op_sel_hi:[1,1,0]
	v_pk_fma_f32 v[242:243], v[238:239], v[232:233], 1.0 op_sel_hi:[1,1,0]
	v_cvt_pk_bf16_f32 v154, v138, v139
	v_cvt_pk_bf16_f32 v155, v140, v141
	v_cvt_pk_bf16_f32 v156, v150, v151
	v_cvt_pk_bf16_f32 v157, v152, v153
	v_cvt_pk_bf16_f32 v158, v184, v185
	v_cvt_pk_bf16_f32 v159, v186, v187
	v_cvt_pk_bf16_f32 v160, v240, v241
	v_cvt_pk_bf16_f32 v161, v242, v243
	ds_read_b128 v[98:101], v172
	ds_read_b128 v[62:65], v172 offset:64
	ds_read_b128 v[94:97], v172 offset:128
	ds_read_b128 v[54:57], v172 offset:192
	v_permlane16_swap_b32_e32 v154, v156
	v_permlane16_swap_b32_e32 v155, v157
	s_cmp_gt_u32 s40, 4
	s_cbranch_scc1 .Lg1_pl9
	global_store_dwordx4 v228, v[154:157], s[60:61] nt
	s_branch .Lg1_dn9
.Lg1_pl9:
	global_store_dwordx4 v228, v[154:157], s[60:61]
.Lg1_dn9:
	v_permlane16_swap_b32_e32 v158, v160
	v_permlane16_swap_b32_e32 v159, v161
	s_cmp_gt_u32 s40, 4
	s_cbranch_scc1 .Lg1_pl10
	global_store_dwordx4 v228, v[158:161], s[60:61] offset:128 nt
	s_branch .Lg1_dn10
.Lg1_pl10:
	global_store_dwordx4 v228, v[158:161], s[60:61] offset:128
.Lg1_dn10:
	v_exp_f32_e32 v130, v82
	v_exp_f32_e32 v131, v83
	v_exp_f32_e32 v132, v84
	v_exp_f32_e32 v133, v85
	v_exp_f32_e32 v142, v34
	v_exp_f32_e32 v143, v35
	v_exp_f32_e32 v144, v36
	v_exp_f32_e32 v145, v37
	v_exp_f32_e32 v176, v118
	v_exp_f32_e32 v177, v119
	v_exp_f32_e32 v178, v120
	v_exp_f32_e32 v179, v121
	v_exp_f32_e32 v232, v46
	v_exp_f32_e32 v233, v47
	v_exp_f32_e32 v234, v48
	v_exp_f32_e32 v235, v49
	v_pk_fma_f32 v[130:131], v[130:131], -0.5, -0.5 op_sel_hi:[1,0,0]
	v_pk_fma_f32 v[132:133], v[132:133], -0.5, -0.5 op_sel_hi:[1,0,0]
	v_pk_fma_f32 v[142:143], v[142:143], -0.5, -0.5 op_sel_hi:[1,0,0]
	v_pk_fma_f32 v[144:145], v[144:145], -0.5, -0.5 op_sel_hi:[1,0,0]
	v_pk_fma_f32 v[176:177], v[176:177], -0.5, -0.5 op_sel_hi:[1,0,0]
	v_pk_fma_f32 v[178:179], v[178:179], -0.5, -0.5 op_sel_hi:[1,0,0]
	v_pk_fma_f32 v[232:233], v[232:233], -0.5, -0.5 op_sel_hi:[1,0,0]
	v_pk_fma_f32 v[234:235], v[234:235], -0.5, -0.5 op_sel_hi:[1,0,0]
	v_pk_mul_f32 v[134:135], v[130:131], v[132:133]
	v_pk_mul_f32 v[146:147], v[142:143], v[144:145]
	v_pk_mul_f32 v[180:181], v[176:177], v[178:179]
	v_pk_mul_f32 v[236:237], v[232:233], v[234:235]
	v_mul_f32_e32 v138, v134, v135
	v_mul_f32_e32 v150, v146, v147
	v_mul_f32_e32 v184, v180, v181
	v_mul_f32_e32 v240, v236, v237
	v_rcp_f32_e32 v138, v138
	v_rcp_f32_e32 v150, v150
	v_rcp_f32_e32 v184, v184
	v_rcp_f32_e32 v240, v240
	v_pk_add_f32 v[164:165], v[164:165], v[82:83]
	v_pk_add_f32 v[164:165], v[164:165], v[84:85]
	v_pk_add_f32 v[164:165], v[164:165], v[34:35]
	v_pk_add_f32 v[164:165], v[164:165], v[36:37]
	v_pk_add_f32 v[164:165], v[164:165], v[118:119]
	v_pk_add_f32 v[164:165], v[164:165], v[120:121]
	v_pk_add_f32 v[164:165], v[164:165], v[46:47]
	v_pk_add_f32 v[164:165], v[164:165], v[48:49]
	v_pk_mul_f32 v[174:175], v[134:135], v[146:147]
	v_pk_mul_f32 v[174:175], v[174:175], v[180:181]
	v_pk_mul_f32 v[174:175], v[174:175], v[236:237]
	v_pk_mul_f32 v[136:137], v[138:139], v[134:135] op_sel:[0,1] op_sel_hi:[0,0]
	v_pk_mul_f32 v[148:149], v[150:151], v[146:147] op_sel:[0,1] op_sel_hi:[0,0]
	v_pk_mul_f32 v[182:183], v[184:185], v[180:181] op_sel:[0,1] op_sel_hi:[0,0]
	v_pk_mul_f32 v[238:239], v[240:241], v[236:237] op_sel:[0,1] op_sel_hi:[0,0]
	v_pk_fma_f32 v[138:139], v[136:137], v[132:133], 1.0 op_sel_hi:[1,1,0]
	v_pk_fma_f32 v[140:141], v[136:137], v[130:131], 1.0 op_sel_hi:[1,1,0]
	v_pk_fma_f32 v[150:151], v[148:149], v[144:145], 1.0 op_sel_hi:[1,1,0]
	v_pk_fma_f32 v[152:153], v[148:149], v[142:143], 1.0 op_sel_hi:[1,1,0]
	v_pk_fma_f32 v[184:185], v[182:183], v[178:179], 1.0 op_sel_hi:[1,1,0]
	v_pk_fma_f32 v[186:187], v[182:183], v[176:177], 1.0 op_sel_hi:[1,1,0]
	v_pk_fma_f32 v[240:241], v[238:239], v[234:235], 1.0 op_sel_hi:[1,1,0]
	v_pk_fma_f32 v[242:243], v[238:239], v[232:233], 1.0 op_sel_hi:[1,1,0]
	v_cvt_pk_bf16_f32 v154, v138, v139
	v_cvt_pk_bf16_f32 v155, v140, v141
	v_cvt_pk_bf16_f32 v156, v150, v151
	v_cvt_pk_bf16_f32 v157, v152, v153
	v_cvt_pk_bf16_f32 v158, v184, v185
	v_cvt_pk_bf16_f32 v159, v186, v187
	v_cvt_pk_bf16_f32 v160, v240, v241
	v_cvt_pk_bf16_f32 v161, v242, v243
	ds_read_b128 v[82:85], v172 offset:512
	ds_read_b128 v[34:37], v172 offset:576
	ds_read_b128 v[118:121], v172 offset:640
	ds_read_b128 v[46:49], v172 offset:704
	v_permlane16_swap_b32_e32 v154, v156
	v_permlane16_swap_b32_e32 v155, v157
	s_cmp_gt_u32 s40, 4
	s_cbranch_scc1 .Lg1_pl11
	global_store_dwordx4 v228, v[154:157], s[64:65] nt
	s_branch .Lg1_dn11
.Lg1_pl11:
	global_store_dwordx4 v228, v[154:157], s[64:65]
.Lg1_dn11:
	v_permlane16_swap_b32_e32 v158, v160
	v_permlane16_swap_b32_e32 v159, v161
	s_cmp_gt_u32 s40, 4
	s_cbranch_scc1 .Lg1_pl12
	global_store_dwordx4 v228, v[158:161], s[64:65] offset:128 nt
	s_branch .Lg1_dn12
.Lg1_pl12:
	global_store_dwordx4 v228, v[158:161], s[64:65] offset:128
.Lg1_dn12:
	v_log_f32_e32 v166, v162
	v_log_f32_e32 v167, v163
	v_log_f32_e32 v170, v174
	v_log_f32_e32 v171, v175
	v_add_f32_e32 v168, v164, v165
	v_mul_f32_e32 v168, 0xbeb17218, v168
	v_add_f32_e32 v166, v166, v167
	v_add_f32_e32 v170, v170, v171
	v_add_f32_e32 v166, v166, v170
	v_fmac_f32_e32 v168, 0x3f317218, v166
	v_mov_b32_e32 v169, v168
	s_nop 1
	v_permlane16_swap_b32_e32 v168, v169
	v_add_f32_e32 v168, v168, v169
	v_mov_b32_e32 v169, v168
	s_nop 1
	v_permlane32_swap_b32_e32 v168, v169
	v_add_f32_e32 v168, v168, v169
	s_mov_b64 exec, s[0:1]
	global_store_dword v229, v168, s[66:67] offset:512
	s_mov_b64 exec, -1
	v_exp_f32_e32 v130, v18
	v_exp_f32_e32 v131, v19
	v_exp_f32_e32 v132, v20
	v_exp_f32_e32 v133, v21
	v_exp_f32_e32 v142, v2
	v_exp_f32_e32 v143, v3
	v_exp_f32_e32 v144, v4
	v_exp_f32_e32 v145, v5
	v_exp_f32_e32 v176, v26
	v_exp_f32_e32 v177, v27
	v_exp_f32_e32 v178, v28
	v_exp_f32_e32 v179, v29
	v_exp_f32_e32 v232, v10
	v_exp_f32_e32 v233, v11
	v_exp_f32_e32 v234, v12
	v_exp_f32_e32 v235, v13
	v_pk_fma_f32 v[130:131], v[130:131], -0.5, -0.5 op_sel_hi:[1,0,0]
	v_pk_fma_f32 v[132:133], v[132:133], -0.5, -0.5 op_sel_hi:[1,0,0]
	v_pk_fma_f32 v[142:143], v[142:143], -0.5, -0.5 op_sel_hi:[1,0,0]
	v_pk_fma_f32 v[144:145], v[144:145], -0.5, -0.5 op_sel_hi:[1,0,0]
	v_pk_fma_f32 v[176:177], v[176:177], -0.5, -0.5 op_sel_hi:[1,0,0]
	v_pk_fma_f32 v[178:179], v[178:179], -0.5, -0.5 op_sel_hi:[1,0,0]
	v_pk_fma_f32 v[232:233], v[232:233], -0.5, -0.5 op_sel_hi:[1,0,0]
	v_pk_fma_f32 v[234:235], v[234:235], -0.5, -0.5 op_sel_hi:[1,0,0]
	v_pk_mul_f32 v[134:135], v[130:131], v[132:133]
	v_pk_mul_f32 v[146:147], v[142:143], v[144:145]
	v_pk_mul_f32 v[180:181], v[176:177], v[178:179]
	v_pk_mul_f32 v[236:237], v[232:233], v[234:235]
	v_mul_f32_e32 v138, v134, v135
	v_mul_f32_e32 v150, v146, v147
	v_mul_f32_e32 v184, v180, v181
	v_mul_f32_e32 v240, v236, v237
	v_rcp_f32_e32 v138, v138
	v_rcp_f32_e32 v150, v150
	v_rcp_f32_e32 v184, v184
	v_rcp_f32_e32 v240, v240
	v_pk_add_f32 v[164:165], v[18:19], v[20:21]
	v_pk_add_f32 v[164:165], v[164:165], v[2:3]
	v_pk_add_f32 v[164:165], v[164:165], v[4:5]
	v_pk_add_f32 v[164:165], v[164:165], v[26:27]
	v_pk_add_f32 v[164:165], v[164:165], v[28:29]
	v_pk_add_f32 v[164:165], v[164:165], v[10:11]
	v_pk_add_f32 v[164:165], v[164:165], v[12:13]
	v_pk_mul_f32 v[162:163], v[134:135], v[146:147]
	v_pk_mul_f32 v[162:163], v[162:163], v[180:181]
	v_pk_mul_f32 v[162:163], v[162:163], v[236:237]
	v_pk_mul_f32 v[136:137], v[138:139], v[134:135] op_sel:[0,1] op_sel_hi:[0,0]
	v_pk_mul_f32 v[148:149], v[150:151], v[146:147] op_sel:[0,1] op_sel_hi:[0,0]
	v_pk_mul_f32 v[182:183], v[184:185], v[180:181] op_sel:[0,1] op_sel_hi:[0,0]
	v_pk_mul_f32 v[238:239], v[240:241], v[236:237] op_sel:[0,1] op_sel_hi:[0,0]
	v_pk_fma_f32 v[138:139], v[136:137], v[132:133], 1.0 op_sel_hi:[1,1,0]
	v_pk_fma_f32 v[140:141], v[136:137], v[130:131], 1.0 op_sel_hi:[1,1,0]
	v_pk_fma_f32 v[150:151], v[148:149], v[144:145], 1.0 op_sel_hi:[1,1,0]
	v_pk_fma_f32 v[152:153], v[148:149], v[142:143], 1.0 op_sel_hi:[1,1,0]
	v_pk_fma_f32 v[184:185], v[182:183], v[178:179], 1.0 op_sel_hi:[1,1,0]
	v_pk_fma_f32 v[186:187], v[182:183], v[176:177], 1.0 op_sel_hi:[1,1,0]
	v_pk_fma_f32 v[240:241], v[238:239], v[234:235], 1.0 op_sel_hi:[1,1,0]
	v_pk_fma_f32 v[242:243], v[238:239], v[232:233], 1.0 op_sel_hi:[1,1,0]
	v_cvt_pk_bf16_f32 v154, v138, v139
	v_cvt_pk_bf16_f32 v155, v140, v141
	v_cvt_pk_bf16_f32 v156, v150, v151
	v_cvt_pk_bf16_f32 v157, v152, v153
	v_cvt_pk_bf16_f32 v158, v184, v185
	v_cvt_pk_bf16_f32 v159, v186, v187
	v_cvt_pk_bf16_f32 v160, v240, v241
	v_cvt_pk_bf16_f32 v161, v242, v243
	ds_read_b128 v[18:21], v172
	ds_read_b128 v[2:5], v172 offset:64
	ds_read_b128 v[26:29], v172 offset:128
	ds_read_b128 v[10:13], v172 offset:192
	v_permlane16_swap_b32_e32 v154, v156
	v_permlane16_swap_b32_e32 v155, v157
	s_cmp_gt_u32 s40, 4
	s_cbranch_scc1 .Lg1_pl13
	global_store_dwordx4 v228, v[154:157], s[60:61] offset:2048 nt
	s_branch .Lg1_dn13
.Lg1_pl13:
	global_store_dwordx4 v228, v[154:157], s[60:61] offset:2048
.Lg1_dn13:
	v_permlane16_swap_b32_e32 v158, v160
	v_permlane16_swap_b32_e32 v159, v161
	s_cmp_gt_u32 s40, 4
	s_cbranch_scc1 .Lg1_pl14
	global_store_dwordx4 v228, v[158:161], s[60:61] offset:2176 nt
	s_branch .Lg1_dn14
.Lg1_pl14:
	global_store_dwordx4 v228, v[158:161], s[60:61] offset:2176
.Lg1_dn14:
	v_exp_f32_e32 v130, v22
	v_exp_f32_e32 v131, v23
	v_exp_f32_e32 v132, v24
	v_exp_f32_e32 v133, v25
	v_exp_f32_e32 v142, v6
	v_exp_f32_e32 v143, v7
	v_exp_f32_e32 v144, v8
	v_exp_f32_e32 v145, v9
	v_exp_f32_e32 v176, v30
	v_exp_f32_e32 v177, v31
	v_exp_f32_e32 v178, v32
	v_exp_f32_e32 v179, v33
	v_exp_f32_e32 v232, v14
	v_exp_f32_e32 v233, v15
	v_exp_f32_e32 v234, v16
	v_exp_f32_e32 v235, v17
	v_pk_fma_f32 v[130:131], v[130:131], -0.5, -0.5 op_sel_hi:[1,0,0]
	v_pk_fma_f32 v[132:133], v[132:133], -0.5, -0.5 op_sel_hi:[1,0,0]
	v_pk_fma_f32 v[142:143], v[142:143], -0.5, -0.5 op_sel_hi:[1,0,0]
	v_pk_fma_f32 v[144:145], v[144:145], -0.5, -0.5 op_sel_hi:[1,0,0]
	v_pk_fma_f32 v[176:177], v[176:177], -0.5, -0.5 op_sel_hi:[1,0,0]
	v_pk_fma_f32 v[178:179], v[178:179], -0.5, -0.5 op_sel_hi:[1,0,0]
	v_pk_fma_f32 v[232:233], v[232:233], -0.5, -0.5 op_sel_hi:[1,0,0]
	v_pk_fma_f32 v[234:235], v[234:235], -0.5, -0.5 op_sel_hi:[1,0,0]
	v_pk_mul_f32 v[134:135], v[130:131], v[132:133]
	v_pk_mul_f32 v[146:147], v[142:143], v[144:145]
	v_pk_mul_f32 v[180:181], v[176:177], v[178:179]
	v_pk_mul_f32 v[236:237], v[232:233], v[234:235]
	v_mul_f32_e32 v138, v134, v135
	v_mul_f32_e32 v150, v146, v147
	v_mul_f32_e32 v184, v180, v181
	v_mul_f32_e32 v240, v236, v237
	v_rcp_f32_e32 v138, v138
	v_rcp_f32_e32 v150, v150
	v_rcp_f32_e32 v184, v184
	v_rcp_f32_e32 v240, v240
	v_pk_add_f32 v[164:165], v[164:165], v[22:23]
	v_pk_add_f32 v[164:165], v[164:165], v[24:25]
	v_pk_add_f32 v[164:165], v[164:165], v[6:7]
	v_pk_add_f32 v[164:165], v[164:165], v[8:9]
	v_pk_add_f32 v[164:165], v[164:165], v[30:31]
	v_pk_add_f32 v[164:165], v[164:165], v[32:33]
	v_pk_add_f32 v[164:165], v[164:165], v[14:15]
	v_pk_add_f32 v[164:165], v[164:165], v[16:17]
	v_pk_mul_f32 v[174:175], v[134:135], v[146:147]
	v_pk_mul_f32 v[174:175], v[174:175], v[180:181]
	v_pk_mul_f32 v[174:175], v[174:175], v[236:237]
	v_pk_mul_f32 v[136:137], v[138:139], v[134:135] op_sel:[0,1] op_sel_hi:[0,0]
	v_pk_mul_f32 v[148:149], v[150:151], v[146:147] op_sel:[0,1] op_sel_hi:[0,0]
	v_pk_mul_f32 v[182:183], v[184:185], v[180:181] op_sel:[0,1] op_sel_hi:[0,0]
	v_pk_mul_f32 v[238:239], v[240:241], v[236:237] op_sel:[0,1] op_sel_hi:[0,0]
	v_pk_fma_f32 v[138:139], v[136:137], v[132:133], 1.0 op_sel_hi:[1,1,0]
	v_pk_fma_f32 v[140:141], v[136:137], v[130:131], 1.0 op_sel_hi:[1,1,0]
	v_pk_fma_f32 v[150:151], v[148:149], v[144:145], 1.0 op_sel_hi:[1,1,0]
	v_pk_fma_f32 v[152:153], v[148:149], v[142:143], 1.0 op_sel_hi:[1,1,0]
	v_pk_fma_f32 v[184:185], v[182:183], v[178:179], 1.0 op_sel_hi:[1,1,0]
	v_pk_fma_f32 v[186:187], v[182:183], v[176:177], 1.0 op_sel_hi:[1,1,0]
	v_pk_fma_f32 v[240:241], v[238:239], v[234:235], 1.0 op_sel_hi:[1,1,0]
	v_pk_fma_f32 v[242:243], v[238:239], v[232:233], 1.0 op_sel_hi:[1,1,0]
	v_cvt_pk_bf16_f32 v154, v138, v139
	v_cvt_pk_bf16_f32 v155, v140, v141
	v_cvt_pk_bf16_f32 v156, v150, v151
	v_cvt_pk_bf16_f32 v157, v152, v153
	v_cvt_pk_bf16_f32 v158, v184, v185
	v_cvt_pk_bf16_f32 v159, v186, v187
	v_cvt_pk_bf16_f32 v160, v240, v241
	v_cvt_pk_bf16_f32 v161, v242, v243
	ds_read_b128 v[22:25], v172 offset:512
	ds_read_b128 v[6:9], v172 offset:576
	ds_read_b128 v[30:33], v172 offset:640
	ds_read_b128 v[14:17], v172 offset:704
	v_permlane16_swap_b32_e32 v154, v156
	v_permlane16_swap_b32_e32 v155, v157
	s_cmp_gt_u32 s40, 4
	s_cbranch_scc1 .Lg1_pl15
	global_store_dwordx4 v228, v[154:157], s[64:65] offset:2048 nt
	s_branch .Lg1_dn15
.Lg1_pl15:
	global_store_dwordx4 v228, v[154:157], s[64:65] offset:2048
.Lg1_dn15:
	v_permlane16_swap_b32_e32 v158, v160
	v_permlane16_swap_b32_e32 v159, v161
	s_cmp_gt_u32 s40, 4
	s_cbranch_scc1 .Lg1_pl16
	global_store_dwordx4 v228, v[158:161], s[64:65] offset:2176 nt
	s_branch .Lg1_dn16
.Lg1_pl16:
	global_store_dwordx4 v228, v[158:161], s[64:65] offset:2176
.Lg1_dn16:
	v_log_f32_e32 v166, v162
	v_log_f32_e32 v167, v163
	v_log_f32_e32 v170, v174
	v_log_f32_e32 v171, v175
	v_add_f32_e32 v168, v164, v165
	v_mul_f32_e32 v168, 0xbeb17218, v168
	v_add_f32_e32 v166, v166, v167
	v_add_f32_e32 v170, v170, v171
	v_add_f32_e32 v166, v166, v170
	v_fmac_f32_e32 v168, 0x3f317218, v166
	v_mov_b32_e32 v169, v168
	s_nop 1
	v_permlane16_swap_b32_e32 v168, v169
	v_add_f32_e32 v168, v168, v169
	v_mov_b32_e32 v169, v168
	s_nop 1
	v_permlane32_swap_b32_e32 v168, v169
	v_add_f32_e32 v168, v168, v169
	s_mov_b64 exec, s[0:1]
	global_store_dword v229, v168, s[66:67] offset:576
	s_mov_b64 exec, -1
	s_bitcmp1_b32 s20, 12
	s_cbranch_scc0 .Lg1_noY
	s_barrier
